# baseline (speedup 1.0000x reference)
_Z17conv_xproj_kernelPKDF16_PKfS2_S0_PDF16_S3_Pf:
	s_load_dwordx8 s[4:11], s[0:1], 0x0
	s_load_dwordx2 s[14:15], s[0:1], 0x20
	s_lshl_b32 s12, s2, 4
	s_getreg_b32 s16, hwreg(HW_REG_HW_ID, 0, 4)
	s_and_b32 s16, s16, 3
	s_cmp_eq_u32 s16, 0
	s_cbranch_scc1 .Lstag_cx_done
.Lstag_cx_loop:
	s_sleep 3
	s_sub_u32 s16, s16, 1
	s_cmp_lg_u32 s16, 0
	s_cbranch_scc1 .Lstag_cx_loop
.Lstag_cx_done:
	s_and_b32 s3, s2, 0x7f
	v_lshlrev_b32_e32 v60, 4, v0
	v_lshrrev_b32_e32 v61, 6, v0
	v_and_b32_e32 v59, 63, v0
	v_mul_u32_u24_e32 v58, 0x600, v61
	v_or_b32_e32 v59, v58, v59
	v_lshlrev_b32_e32 v59, 4, v59
	s_waitcnt lgkmcnt(0)
	s_lshl_b32 s13, s2, 17
	s_add_u32 s16, s4, s13
	s_addc_u32 s17, s5, 0
	s_cmp_eq_u32 s3, 0
	s_cbranch_scc1 .Lcx_first
	s_sub_u32 s18, s16, 0x8000
	s_subb_u32 s19, s17, 0
	global_load_dwordx4 v[2:5], v60, s[18:19]
	s_branch .Lcx_go
